# strategy 7: DPP wave scans (row_shr/row_bcast) replace ds_bpermute scans in k_localsort and k_bucketsort
# speedup vs baseline: 1.0111x; 1.0057x over previous
.LBB1_45:
	s_or_b64 exec, exec, s[38:39]
	v_mov_b32_e32 v85, 0
	s_waitcnt lgkmcnt(0)
	s_barrier
	s_and_saveexec_b64 s[38:39], s[50:51]
	ds_read_b32 v85, v38
	s_or_b64 exec, exec, s[38:39]
	s_waitcnt lgkmcnt(0)
	v_mov_b32_e32 v86, v85
	v_and_b32_e32 v92, 63, v0
	v_lshrrev_b32_e32 v90, 6, v0
	v_add_u32_dpp v86, v86, v86 row_shr:1 row_mask:0xf bank_mask:0xf
	v_lshlrev_b32_e32 v90, 2, v90
	v_cmp_eq_u32_e64 s[52:53], 63, v92
	v_add_u32_dpp v86, v86, v86 row_shr:2 row_mask:0xf bank_mask:0xf
	v_cmp_lt_u32_e64 s[48:49], 63, v0
	v_cmp_gt_u32_e64 s[54:55], 16, v0
	v_add_u32_dpp v86, v86, v86 row_shr:4 row_mask:0xf bank_mask:0xf
	s_nop 1
	v_add_u32_dpp v86, v86, v86 row_shr:8 row_mask:0xf bank_mask:0xf
	s_nop 1
	v_add_u32_dpp v86, v86, v86 row_bcast:15 row_mask:0xa bank_mask:0xf
	s_nop 1
	v_add_u32_dpp v86, v86, v86 row_bcast:31 row_mask:0xc bank_mask:0xf
	s_and_saveexec_b64 s[46:47], s[52:53]
	ds_write_b32 v90, v86 offset:1568
	s_mov_b64 exec, s[46:47]
	s_waitcnt lgkmcnt(0)
	s_barrier
	s_and_saveexec_b64 s[46:47], s[54:55]
	s_cbranch_execz .Lls_scan2_done
	v_lshlrev_b32_e32 v92, 2, v92
	ds_read_b32 v87, v92 offset:1568
	s_waitcnt lgkmcnt(0)
	s_nop 1
	v_add_u32_dpp v87, v87, v87 row_shr:1 row_mask:0xf bank_mask:0xf
	s_nop 1
	v_add_u32_dpp v87, v87, v87 row_shr:2 row_mask:0xf bank_mask:0xf
	s_nop 1
	v_add_u32_dpp v87, v87, v87 row_shr:4 row_mask:0xf bank_mask:0xf
	s_nop 1
	v_add_u32_dpp v87, v87, v87 row_shr:8 row_mask:0xf bank_mask:0xf
	ds_write_b32 v92, v87 offset:1632
.Lls_scan2_done:
	s_or_b64 exec, exec, s[46:47]
	v_mov_b32_e32 v87, 0
	s_waitcnt lgkmcnt(0)
	v_mov_b32_e32 v88, 0
	s_barrier
	s_and_saveexec_b64 s[38:39], s[48:49]
	ds_read_b32 v88, v90 offset:1628
	s_or_b64 exec, exec, s[38:39]
	ds_read_b32 v87, v87 offset:1692
	s_mul_i32 s40, s2, 0x188
	s_and_saveexec_b64 s[38:39], s[50:51]
	s_cbranch_execz .LBB1_58
	v_sub_u32_e32 v85, v86, v85
	s_waitcnt lgkmcnt(1)
	v_add_u32_e32 v85, v88, v85
	v_add_u32_e32 v88, s40, v0
	v_mov_b32_e32 v89, 0
	v_lshl_add_u64 v[88:89], v[88:89], 2, s[60:61]
	ds_write_b32 v38, v85
	global_store_dword v[88:89], v85, off

.LBB2_119:
	s_or_b64 exec, exec, s[22:23]
	v_mov_b32_e32 v4, 0
	s_waitcnt lgkmcnt(0)
	s_barrier
	s_and_saveexec_b64 s[18:19], vcc
	v_lshlrev_b32_e32 v4, 2, v0
	ds_read_b32 v4, v4 offset:49152
	s_or_b64 exec, exec, s[18:19]
	s_waitcnt lgkmcnt(0)
	v_mov_b32_e32 v5, v4
	s_nop 1
	v_add_u32_dpp v5, v5, v5 row_shr:1 row_mask:0xf bank_mask:0xf
	s_nop 1
	v_add_u32_dpp v5, v5, v5 row_shr:2 row_mask:0xf bank_mask:0xf
	s_nop 1
	v_add_u32_dpp v5, v5, v5 row_shr:4 row_mask:0xf bank_mask:0xf
	s_nop 1
	v_add_u32_dpp v5, v5, v5 row_shr:8 row_mask:0xf bank_mask:0xf
	s_nop 1
	v_add_u32_dpp v5, v5, v5 row_bcast:15 row_mask:0xa bank_mask:0xf
	s_nop 1
	v_add_u32_dpp v5, v5, v5 row_bcast:31 row_mask:0xc bank_mask:0xf
	s_and_saveexec_b64 s[18:19], s[14:15]
	ds_write_b32 v8, v5 offset:54016
	s_or_b64 exec, exec, s[18:19]
	s_waitcnt lgkmcnt(0)
	s_barrier
	s_and_saveexec_b64 s[14:15], s[16:17]
	s_cbranch_execz .LBB2_128
	v_mov_b32_e32 v44, 0
	v_lshlrev_b32_e32 v43, 2, v2
	s_and_saveexec_b64 s[16:17], s[10:11]
	ds_read_b32 v44, v43 offset:54016
	s_or_b64 exec, exec, s[16:17]
	s_waitcnt lgkmcnt(0)
	v_mov_b32_e32 v3, v44
	s_nop 1
	v_add_u32_dpp v3, v3, v3 row_shr:1 row_mask:0xf bank_mask:0xf
	s_nop 1
	v_add_u32_dpp v3, v3, v3 row_shr:2 row_mask:0xf bank_mask:0xf
	s_nop 1
	v_add_u32_dpp v3, v3, v3 row_shr:4 row_mask:0xf bank_mask:0xf
	s_nop 1
	v_add_u32_dpp v3, v3, v3 row_shr:8 row_mask:0xf bank_mask:0xf
	s_and_b64 exec, exec, s[10:11]
	ds_write_b32 v43, v3 offset:54080
